# conv item loop: all of an item's loads issued with the first batch (fresh regs + copy-back), loop-top store drain removed (on top of v30)
# baseline (speedup 1.0000x reference)
.LBB0_783:
	s_or_b64 exec, exec, s[44:45]
	v_lshlrev_b32_e32 v60, 2, v34
	v_mov_b32_e32 v61, v1
	v_lshl_add_u64 v[58:59], s[36:37], 0, v[60:61]
	s_mov_b64 s[0:1], 0x1000
	s_waitcnt vmcnt(6)
	v_lshlrev_b32_e32 v94, 16, v30
	v_and_b32_e32 v97, 0xffff0000, v31
	v_and_b32_e32 v96, 0xffff0000, v30
	v_lshlrev_b32_e32 v95, 16, v31
	s_waitcnt vmcnt(5)
	v_lshlrev_b32_e32 v31, 16, v23
	v_lshlrev_b32_e32 v30, 16, v22
	v_and_b32_e32 v107, 0xffff0000, v23
	v_and_b32_e32 v106, 0xffff0000, v22
	v_lshl_add_u64 v[22:23], v[58:59], 0, s[0:1]
	v_readlane_b32 s0, v252, 28
	v_readlane_b32 s1, v252, 29
	v_lshlrev_b32_e32 v90, 16, v26
	v_and_b32_e32 v93, 0xffff0000, v27
	v_and_b32_e32 v92, 0xffff0000, v26
	v_lshlrev_b32_e32 v91, 16, v27
	v_mov_b64_e32 v[26:27], s[0:1]
	s_movk_i32 s4, 0xc00
	v_lshlrev_b32_e32 v74, 16, v28
	v_and_b32_e32 v77, 0xffff0000, v29
	v_and_b32_e32 v76, 0xffff0000, v28
	v_lshlrev_b32_e32 v75, 16, v29
	v_mad_i64_i32 v[28:29], s[0:1], v43, s4, v[26:27]
	v_lshlrev_b32_e32 v87, 16, v40
	v_and_b32_e32 v89, 0xffff0000, v40
	v_lshlrev_b32_e32 v40, 16, v48
	v_and_b32_e32 v72, 0xffff0000, v48
	s_waitcnt vmcnt(0)
	v_lshlrev_b32_e32 v118, 16, v49
	v_and_b32_e32 v122, 0xffff0000, v49
	v_lshl_add_u64 v[48:49], v[28:29], 0, v[0:1]
	v_or_b32_e32 v28, 1, v43
	v_mad_i64_i32 v[28:29], s[0:1], v28, s4, v[26:27]
	v_lshlrev_b32_e32 v80, 16, v36
	v_and_b32_e32 v84, 0xffff0000, v36
	v_lshlrev_b32_e32 v34, 16, v41
	v_and_b32_e32 v36, 0xffff0000, v41
	v_lshlrev_b32_e32 v41, 16, v47
	v_and_b32_e32 v73, 0xffff0000, v47
	v_and_b32_e32 v83, 0xffff0000, v33
	v_lshlrev_b32_e32 v79, 16, v33
	v_lshlrev_b32_e32 v105, 16, v19
	v_and_b32_e32 v109, 0xffff0000, v19
	v_lshlrev_b32_e32 v33, 16, v25
	v_lshlrev_b32_e32 v99, 16, v21
	v_and_b32_e32 v101, 0xffff0000, v25
	v_and_b32_e32 v103, 0xffff0000, v21
	v_and_b32_e32 v21, 0xffff0000, v11
	v_and_b32_e32 v51, 0xffff0000, v15
	v_lshlrev_b32_e32 v19, 16, v11
	v_lshlrev_b32_e32 v25, 16, v15
	v_and_b32_e32 v67, 0xffff0000, v13
	v_and_b32_e32 v71, 0xffff0000, v17
	v_lshlrev_b32_e32 v63, 16, v13
	v_lshlrev_b32_e32 v69, 16, v17
	v_and_b32_e32 v13, 0xffff0000, v3
	v_and_b32_e32 v17, 0xffff0000, v7
	v_lshlrev_b32_e32 v11, 16, v3
	v_lshlrev_b32_e32 v15, 16, v7
	v_lshlrev_b32_e32 v3, 16, v46
	v_and_b32_e32 v7, 0xffff0000, v46
	v_lshl_add_u64 v[46:47], v[28:29], 0, v[0:1]
	v_or_b32_e32 v28, 2, v43
	v_mad_i64_i32 v[28:29], s[0:1], v28, s4, v[26:27]
	v_lshlrev_b32_e32 v86, 16, v44
	v_and_b32_e32 v88, 0xffff0000, v44
	v_lshlrev_b32_e32 v78, 16, v32
	v_and_b32_e32 v82, 0xffff0000, v32
	v_lshlrev_b32_e32 v104, 16, v18
	v_and_b32_e32 v108, 0xffff0000, v18
	v_lshlrev_b32_e32 v32, 16, v24
	v_lshlrev_b32_e32 v98, 16, v20
	v_and_b32_e32 v100, 0xffff0000, v24
	v_and_b32_e32 v102, 0xffff0000, v20
	v_lshlrev_b32_e32 v18, 16, v10
	v_lshlrev_b32_e32 v24, 16, v14
	v_and_b32_e32 v20, 0xffff0000, v10
	v_and_b32_e32 v50, 0xffff0000, v14
	v_lshlrev_b32_e32 v62, 16, v12
	v_lshlrev_b32_e32 v68, 16, v16
	v_and_b32_e32 v66, 0xffff0000, v12
	v_and_b32_e32 v70, 0xffff0000, v16
	v_lshlrev_b32_e32 v10, 16, v2
	v_lshlrev_b32_e32 v14, 16, v6
	v_and_b32_e32 v12, 0xffff0000, v2
	v_and_b32_e32 v16, 0xffff0000, v6
	v_lshlrev_b32_e32 v2, 16, v45
	v_and_b32_e32 v6, 0xffff0000, v45
	v_lshl_add_u64 v[44:45], v[28:29], 0, v[0:1]
	v_or_b32_e32 v28, 3, v42
	v_mad_i64_i32 v[26:27], s[0:1], v28, s4, v[26:27]
	s_mov_b32 s0, 0xa000
	v_lshl_add_u64 v[42:43], v[26:27], 0, v[0:1]
	v_add_co_u32_e32 v26, vcc, s0, v38
	v_lshlrev_b32_e32 v110, 16, v4
	v_lshlrev_b32_e32 v114, 16, v8
	v_and_b32_e32 v113, 0xffff0000, v5
	v_and_b32_e32 v112, 0xffff0000, v4
	v_and_b32_e32 v117, 0xffff0000, v9
	v_and_b32_e32 v116, 0xffff0000, v8
	v_lshlrev_b32_e32 v111, 16, v5
	v_lshlrev_b32_e32 v115, 16, v9
	v_lshlrev_b32_e32 v5, 16, v54
	v_lshlrev_b32_e32 v4, 16, v53
	v_and_b32_e32 v9, 0xffff0000, v54
	v_and_b32_e32 v8, 0xffff0000, v53
	v_addc_co_u32_e32 v27, vcc, 0, v39, vcc
	v_lshlrev_b32_e32 v119, 16, v52
	v_lshlrev_b32_e32 v121, 16, v56
	v_and_b32_e32 v123, 0xffff0000, v52
	v_and_b32_e32 v125, 0xffff0000, v56
	v_pk_mul_f32 v[56:57], v[20:21], v[50:51]
	v_pk_mul_f32 v[52:53], v[10:11], v[14:15]
	v_pk_mul_f32 v[50:51], v[12:13], v[16:17]
	v_pk_mul_f32 v[128:129], v[2:3], v[4:5]
	v_pk_mul_f32 v[126:127], v[6:7], v[8:9]
	s_movk_i32 s0, 0x1000
	v_lshlrev_b32_e32 v120, 16, v55
	v_and_b32_e32 v124, 0xffff0000, v55
	v_pk_mul_f32 v[54:55], v[18:19], v[24:25]
	v_add_co_u32_e32 v18, vcc, s0, v58
	v_lshlrev_b32_e32 v81, 16, v35
	s_nop 0
	v_addc_co_u32_e32 v19, vcc, 0, v59, vcc
	s_nop 0
	v_and_b32_e32 v85, 0xffff0000, v35
	v_lshlrev_b32_e32 v35, 16, v37
	v_and_b32_e32 v37, 0xffff0000, v37
	v_pk_mul_f32 v[34:35], v[34:35], v[40:41]
	v_pk_mul_f32 v[40:41], v[74:75], v[78:79]
	s_movk_i32 s0, 0x3000
	s_waitcnt vmcnt(6)
	v_mov_b64_e32 v[26:27], v[170:171]
	v_mov_b64_e32 v[28:29], v[172:173]
	v_lshlrev_b32_e32 v133, 16, v27
	v_lshlrev_b32_e32 v132, 16, v26
	v_and_b32_e32 v27, 0xffff0000, v27
	v_and_b32_e32 v26, 0xffff0000, v26
	s_waitcnt vmcnt(4)
	v_mov_b64_e32 v[2:3], v[174:175]
	v_mov_b64_e32 v[4:5], v[176:177]
	v_mov_b64_e32 v[10:11], v[178:179]
	v_mov_b64_e32 v[12:13], v[180:181]
	v_mov_b32_e32 v58, v10
	v_mov_b32_e32 v59, v12
	s_waitcnt vmcnt(2)
	v_mov_b64_e32 v[6:7], v[182:183]
	v_mov_b64_e32 v[8:9], v[184:185]
	v_mov_b64_e32 v[14:15], v[186:187]
	v_mov_b64_e32 v[16:17], v[188:189]
	v_mov_b32_e32 v60, v14
	v_mov_b32_e32 v61, v16
	v_mov_b32_e32 v16, v15
	v_pk_mul_f32 v[64:65], v[52:53], v[60:61]
	v_mov_b32_e32 v12, v11
	v_pk_mul_f32 v[10:11], v[50:51], v[16:17]
	v_pk_fma_f32 v[134:135], v[54:55], v[58:59], v[64:65]
	v_pk_fma_f32 v[10:11], v[56:57], v[12:13], v[10:11]
	s_waitcnt vmcnt(1)
	v_mov_b64_e32 v[18:19], v[190:191]
	v_mov_b64_e32 v[20:21], v[192:193]
	v_mov_b32_e32 v65, v20
	v_mov_b32_e32 v20, v19
	v_mov_b32_e32 v64, v18
	v_pk_fma_f32 v[10:11], v[126:127], v[20:21], v[10:11]
	v_pk_fma_f32 v[128:129], v[128:129], v[64:65], v[134:135]
	v_pk_mul_f32 v[10:11], v[10:11], v[26:27]
	v_pk_mul_f32 v[128:129], v[128:129], v[132:133]
	v_and_b32_sdwa v18, v10, v236 dst_sel:DWORD dst_unused:UNUSED_PAD src0_sel:WORD_1 src1_sel:DWORD
	v_and_b32_sdwa v14, v128, v236 dst_sel:DWORD dst_unused:UNUSED_PAD src0_sel:WORD_1 src1_sel:DWORD
	v_add3_u32 v10, v10, v18, s80
	v_add3_u32 v14, v128, v14, s80
	v_and_b32_sdwa v15, v11, v236 dst_sel:DWORD dst_unused:UNUSED_PAD src0_sel:WORD_1 src1_sel:DWORD
	v_and_b32_e32 v10, 0xffff0000, v10
	v_and_b32_sdwa v0, v129, v236 dst_sel:DWORD dst_unused:UNUSED_PAD src0_sel:WORD_1 src1_sel:DWORD
	v_add3_u32 v11, v11, v15, s80
	v_or_b32_sdwa v26, v10, v14 dst_sel:DWORD dst_unused:UNUSED_PAD src0_sel:DWORD src1_sel:WORD_1
	v_pk_mul_f32 v[18:19], v[62:63], v[68:69]
	v_pk_mul_f32 v[14:15], v[110:111], v[114:115]
	v_mov_b32_e32 v68, v6
	v_mov_b32_e32 v69, v8
	v_add3_u32 v0, v129, v0, s80
	v_and_b32_e32 v11, 0xffff0000, v11
	v_pk_mul_f32 v[62:63], v[66:67], v[70:71]
	v_mov_b32_e32 v66, v2
	v_mov_b32_e32 v67, v4
	v_pk_mul_f32 v[70:71], v[14:15], v[68:69]
	v_or_b32_sdwa v27, v11, v0 dst_sel:DWORD dst_unused:UNUSED_PAD src0_sel:DWORD src1_sel:WORD_1
	v_pk_mul_f32 v[10:11], v[112:113], v[116:117]
	v_pk_mul_f32 v[110:111], v[118:119], v[120:121]
	v_pk_fma_f32 v[116:117], v[18:19], v[66:67], v[70:71]
	s_waitcnt vmcnt(0)
	v_mov_b64_e32 v[22:23], v[194:195]
	v_mov_b64_e32 v[24:25], v[196:197]
	v_mov_b32_e32 v70, v22
	v_mov_b32_e32 v71, v24
	v_lshlrev_b32_e32 v115, 16, v29
	v_lshlrev_b32_e32 v114, 16, v28
	v_pk_fma_f32 v[110:111], v[110:111], v[70:71], v[116:117]
	v_mov_b32_e32 v8, v7
	v_pk_mul_f32 v[110:111], v[110:111], v[114:115]
	v_mov_b32_e32 v4, v3
	v_pk_mul_f32 v[2:3], v[10:11], v[8:9]
	v_pk_mul_f32 v[112:113], v[122:123], v[124:125]
	v_pk_fma_f32 v[2:3], v[62:63], v[4:5], v[2:3]
	v_mov_b32_e32 v24, v23
	v_and_b32_sdwa v0, v111, v236 dst_sel:DWORD dst_unused:UNUSED_PAD src0_sel:WORD_1 src1_sel:DWORD
	v_and_b32_sdwa v6, v110, v236 dst_sel:DWORD dst_unused:UNUSED_PAD src0_sel:WORD_1 src1_sel:DWORD
	v_pk_fma_f32 v[2:3], v[112:113], v[24:25], v[2:3]
	v_add3_u32 v6, v110, v6, s80
	v_add3_u32 v0, v111, v0, s80
	v_and_b32_e32 v29, 0xffff0000, v29
	v_and_b32_e32 v28, 0xffff0000, v28
	v_pk_mul_f32 v[2:3], v[2:3], v[28:29]
	s_waitcnt vmcnt(0)
	v_mov_b64_e32 v[110:111], v[198:199]
	v_mov_b64_e32 v[112:113], v[200:201]
	v_and_b32_e32 v75, 0xffff0000, v113
	v_and_b32_sdwa v22, v2, v236 dst_sel:DWORD dst_unused:UNUSED_PAD src0_sel:WORD_1 src1_sel:DWORD
	v_add3_u32 v2, v2, v22, s80
	v_pk_mul_f32 v[22:23], v[80:81], v[86:87]
	v_pk_mul_f32 v[86:87], v[84:85], v[88:89]
	v_pk_mul_f32 v[84:85], v[90:91], v[94:95]
	v_and_b32_sdwa v7, v3, v236 dst_sel:DWORD dst_unused:UNUSED_PAD src0_sel:WORD_1 src1_sel:DWORD
	v_and_b32_e32 v2, 0xffff0000, v2
	v_pk_mul_f32 v[90:91], v[84:85], v[60:61]
	v_add3_u32 v3, v3, v7, s80
	v_or_b32_sdwa v28, v2, v6 dst_sel:DWORD dst_unused:UNUSED_PAD src0_sel:DWORD src1_sel:WORD_1
	v_pk_mul_f32 v[6:7], v[30:31], v[104:105]
	v_pk_fma_f32 v[22:23], v[22:23], v[58:59], v[90:91]
	v_pk_mul_f32 v[80:81], v[92:93], v[96:97]
	v_lshlrev_b32_e32 v31, 16, v111
	v_lshlrev_b32_e32 v30, 16, v110
	v_pk_fma_f32 v[22:23], v[6:7], v[64:65], v[22:23]
	v_and_b32_e32 v3, 0xffff0000, v3
	v_pk_mul_f32 v[22:23], v[22:23], v[30:31]
	v_pk_mul_f32 v[30:31], v[80:81], v[16:17]
	v_or_b32_sdwa v29, v3, v0 dst_sel:DWORD dst_unused:UNUSED_PAD src0_sel:DWORD src1_sel:WORD_1
	v_pk_mul_f32 v[2:3], v[106:107], v[108:109]
	v_pk_fma_f32 v[30:31], v[86:87], v[12:13], v[30:31]
	v_and_b32_e32 v89, 0xffff0000, v111
	v_and_b32_e32 v88, 0xffff0000, v110
	v_pk_fma_f32 v[30:31], v[2:3], v[20:21], v[30:31]
	v_and_b32_sdwa v86, v22, v236 dst_sel:DWORD dst_unused:UNUSED_PAD src0_sel:WORD_1 src1_sel:DWORD
	v_pk_mul_f32 v[30:31], v[30:31], v[88:89]
	v_add3_u32 v22, v22, v86, s80
	v_and_b32_sdwa v86, v30, v236 dst_sel:DWORD dst_unused:UNUSED_PAD src0_sel:WORD_1 src1_sel:DWORD
	v_and_b32_sdwa v0, v23, v236 dst_sel:DWORD dst_unused:UNUSED_PAD src0_sel:WORD_1 src1_sel:DWORD
	v_add3_u32 v30, v30, v86, s80
	v_pk_mul_f32 v[86:87], v[36:37], v[72:73]
	v_pk_mul_f32 v[36:37], v[76:77], v[82:83]
	v_pk_mul_f32 v[76:77], v[40:41], v[68:69]
	v_add3_u32 v0, v23, v0, s80
	v_and_b32_sdwa v23, v31, v236 dst_sel:DWORD dst_unused:UNUSED_PAD src0_sel:WORD_1 src1_sel:DWORD
	v_pk_mul_f32 v[72:73], v[32:33], v[98:99]
	v_pk_fma_f32 v[34:35], v[34:35], v[66:67], v[76:77]
	v_add3_u32 v23, v31, v23, s80
	v_lshlrev_b32_e32 v33, 16, v113
	v_lshlrev_b32_e32 v32, 16, v112
	v_pk_fma_f32 v[34:35], v[72:73], v[70:71], v[34:35]
	v_and_b32_e32 v23, 0xffff0000, v23
	v_and_b32_e32 v30, 0xffff0000, v30
	v_pk_mul_f32 v[32:33], v[34:35], v[32:33]
	v_pk_mul_f32 v[34:35], v[36:37], v[8:9]
	v_or_b32_sdwa v31, v23, v0 dst_sel:DWORD dst_unused:UNUSED_PAD src0_sel:DWORD src1_sel:WORD_1
	v_or_b32_sdwa v30, v30, v22 dst_sel:DWORD dst_unused:UNUSED_PAD src0_sel:DWORD src1_sel:WORD_1
	v_pk_mul_f32 v[22:23], v[100:101], v[102:103]
	v_pk_fma_f32 v[34:35], v[86:87], v[4:5], v[34:35]
	v_and_b32_e32 v74, 0xffff0000, v112
	v_pk_fma_f32 v[34:35], v[22:23], v[24:25], v[34:35]
	v_and_b32_sdwa v0, v33, v236 dst_sel:DWORD dst_unused:UNUSED_PAD src0_sel:WORD_1 src1_sel:DWORD
	v_pk_mul_f32 v[34:35], v[34:35], v[74:75]
	v_and_b32_sdwa v74, v32, v236 dst_sel:DWORD dst_unused:UNUSED_PAD src0_sel:WORD_1 src1_sel:DWORD
	v_add3_u32 v32, v32, v74, s80
	v_and_b32_sdwa v74, v34, v236 dst_sel:DWORD dst_unused:UNUSED_PAD src0_sel:WORD_1 src1_sel:DWORD
	v_add3_u32 v34, v34, v74, s80
	v_and_b32_e32 v34, 0xffff0000, v34
	v_add3_u32 v0, v33, v0, s80
	v_and_b32_sdwa v33, v35, v236 dst_sel:DWORD dst_unused:UNUSED_PAD src0_sel:WORD_1 src1_sel:DWORD
	v_or_b32_sdwa v32, v34, v32 dst_sel:DWORD dst_unused:UNUSED_PAD src0_sel:DWORD src1_sel:WORD_1
	v_add_co_u32_e32 v34, vcc, s0, v38
	v_add3_u32 v33, v35, v33, s80
	s_nop 0
	v_addc_co_u32_e32 v35, vcc, 0, v39, vcc
	v_pk_mul_f32 v[78:79], v[6:7], v[60:61]
	v_and_b32_e32 v33, 0xffff0000, v33
	v_pk_fma_f32 v[78:79], v[84:85], v[58:59], v[78:79]
	v_or_b32_sdwa v33, v33, v0 dst_sel:DWORD dst_unused:UNUSED_PAD src0_sel:DWORD src1_sel:WORD_1
	v_pk_fma_f32 v[78:79], v[54:55], v[64:65], v[78:79]
	s_movk_i32 s0, 0x6000
	v_add_co_u32_e32 v38, vcc, s0, v38
	v_pk_mul_f32 v[54:55], v[54:55], v[60:61]
	s_nop 0
	v_addc_co_u32_e32 v39, vcc, 0, v39, vcc
	v_pk_fma_f32 v[6:7], v[6:7], v[58:59], v[54:55]
	v_readlane_b32 s0, v252, 30
	v_pk_fma_f32 v[6:7], v[52:53], v[64:65], v[6:7]
	s_waitcnt vmcnt(0)
	v_mov_b64_e32 v[74:75], v[202:203]
	v_mov_b64_e32 v[76:77], v[204:205]
	v_lshlrev_b32_e32 v35, 16, v75
	v_lshlrev_b32_e32 v34, 16, v74
	v_pk_mul_f32 v[34:35], v[78:79], v[34:35]
	v_pk_mul_f32 v[78:79], v[2:3], v[16:17]
	v_and_b32_e32 v75, 0xffff0000, v75
	v_pk_fma_f32 v[78:79], v[80:81], v[12:13], v[78:79]
	v_and_b32_e32 v74, 0xffff0000, v74
	v_pk_fma_f32 v[78:79], v[56:57], v[20:21], v[78:79]
	v_and_b32_sdwa v0, v35, v236 dst_sel:DWORD dst_unused:UNUSED_PAD src0_sel:WORD_1 src1_sel:DWORD
	v_pk_mul_f32 v[74:75], v[78:79], v[74:75]
	v_and_b32_sdwa v78, v34, v236 dst_sel:DWORD dst_unused:UNUSED_PAD src0_sel:WORD_1 src1_sel:DWORD
	v_add3_u32 v34, v34, v78, s80
	v_and_b32_sdwa v78, v74, v236 dst_sel:DWORD dst_unused:UNUSED_PAD src0_sel:WORD_1 src1_sel:DWORD
	v_add3_u32 v74, v74, v78, s80
	v_pk_mul_f32 v[78:79], v[72:73], v[68:69]
	v_add3_u32 v0, v35, v0, s80
	v_and_b32_sdwa v35, v75, v236 dst_sel:DWORD dst_unused:UNUSED_PAD src0_sel:WORD_1 src1_sel:DWORD
	v_and_b32_e32 v74, 0xffff0000, v74
	v_pk_fma_f32 v[40:41], v[40:41], v[66:67], v[78:79]
	v_add3_u32 v35, v75, v35, s80
	v_or_b32_sdwa v34, v74, v34 dst_sel:DWORD dst_unused:UNUSED_PAD src0_sel:DWORD src1_sel:WORD_1
	v_lshlrev_b32_e32 v75, 16, v77
	v_lshlrev_b32_e32 v74, 16, v76
	v_pk_fma_f32 v[40:41], v[18:19], v[70:71], v[40:41]
	v_and_b32_e32 v77, 0xffff0000, v77
	v_pk_mul_f32 v[40:41], v[40:41], v[74:75]
	v_pk_mul_f32 v[74:75], v[22:23], v[8:9]
	v_and_b32_e32 v76, 0xffff0000, v76
	v_pk_fma_f32 v[36:37], v[36:37], v[4:5], v[74:75]
	v_and_b32_sdwa v74, v40, v236 dst_sel:DWORD dst_unused:UNUSED_PAD src0_sel:WORD_1 src1_sel:DWORD
	v_pk_fma_f32 v[36:37], v[62:63], v[24:25], v[36:37]
	v_and_b32_e32 v35, 0xffff0000, v35
	v_pk_mul_f32 v[36:37], v[36:37], v[76:77]
	v_add3_u32 v40, v40, v74, s80
	v_and_b32_sdwa v74, v36, v236 dst_sel:DWORD dst_unused:UNUSED_PAD src0_sel:WORD_1 src1_sel:DWORD
	v_or_b32_sdwa v35, v35, v0 dst_sel:DWORD dst_unused:UNUSED_PAD src0_sel:DWORD src1_sel:WORD_1
	v_and_b32_sdwa v0, v41, v236 dst_sel:DWORD dst_unused:UNUSED_PAD src0_sel:WORD_1 src1_sel:DWORD
	v_add3_u32 v36, v36, v74, s80
	v_add3_u32 v0, v41, v0, s80
	v_and_b32_sdwa v41, v37, v236 dst_sel:DWORD dst_unused:UNUSED_PAD src0_sel:WORD_1 src1_sel:DWORD
	v_and_b32_e32 v36, 0xffff0000, v36
	v_add3_u32 v37, v37, v41, s80
	v_or_b32_sdwa v36, v36, v40 dst_sel:DWORD dst_unused:UNUSED_PAD src0_sel:DWORD src1_sel:WORD_1
	v_pk_mul_f32 v[16:17], v[56:57], v[16:17]
	v_and_b32_e32 v37, 0xffff0000, v37
	v_pk_fma_f32 v[2:3], v[2:3], v[12:13], v[16:17]
	v_or_b32_sdwa v37, v37, v0 dst_sel:DWORD dst_unused:UNUSED_PAD src0_sel:DWORD src1_sel:WORD_1
	v_pk_fma_f32 v[2:3], v[50:51], v[20:21], v[2:3]
	v_pk_mul_f32 v[16:17], v[18:19], v[68:69]
	v_pk_mul_f32 v[8:9], v[62:63], v[8:9]
	v_pk_fma_f32 v[16:17], v[72:73], v[66:67], v[16:17]
	v_pk_fma_f32 v[4:5], v[22:23], v[4:5], v[8:9]
	v_pk_fma_f32 v[14:15], v[14:15], v[70:71], v[16:17]
	v_pk_fma_f32 v[4:5], v[10:11], v[24:25], v[4:5]
	v_add_u32_e32 v131, s0, v131
	v_readlane_b32 s0, v253, 44
	v_cmp_le_i32_e32 vcc, s52, v131
	s_or_b64 s[42:43], vcc, s[42:43]
	v_add_u32_e32 v130, s0, v130
	s_waitcnt vmcnt(0)
	v_mov_b64_e32 v[38:39], v[222:223]
	v_mov_b64_e32 v[40:41], v[224:225]
	v_lshlrev_b32_e32 v75, 16, v39
	v_lshlrev_b32_e32 v74, 16, v38
	v_and_b32_e32 v39, 0xffff0000, v39
	v_and_b32_e32 v38, 0xffff0000, v38
	v_pk_mul_f32 v[6:7], v[6:7], v[74:75]
	v_pk_mul_f32 v[2:3], v[2:3], v[38:39]
	v_and_b32_sdwa v12, v6, v236 dst_sel:DWORD dst_unused:UNUSED_PAD src0_sel:WORD_1 src1_sel:DWORD
	v_add3_u32 v6, v6, v12, s80
	v_and_b32_sdwa v12, v2, v236 dst_sel:DWORD dst_unused:UNUSED_PAD src0_sel:WORD_1 src1_sel:DWORD
	v_and_b32_sdwa v0, v7, v236 dst_sel:DWORD dst_unused:UNUSED_PAD src0_sel:WORD_1 src1_sel:DWORD
	v_add3_u32 v2, v2, v12, s80
	v_add3_u32 v0, v7, v0, s80
	v_and_b32_sdwa v7, v3, v236 dst_sel:DWORD dst_unused:UNUSED_PAD src0_sel:WORD_1 src1_sel:DWORD
	v_and_b32_e32 v2, 0xffff0000, v2
	v_add3_u32 v3, v3, v7, s80
	v_or_b32_sdwa v2, v2, v6 dst_sel:DWORD dst_unused:UNUSED_PAD src0_sel:DWORD src1_sel:WORD_1
	v_lshlrev_b32_e32 v7, 16, v41
	v_lshlrev_b32_e32 v6, 16, v40
	v_and_b32_e32 v3, 0xffff0000, v3
	v_and_b32_e32 v13, 0xffff0000, v41
	v_and_b32_e32 v12, 0xffff0000, v40
	v_pk_mul_f32 v[6:7], v[14:15], v[6:7]
	v_or_b32_sdwa v3, v3, v0 dst_sel:DWORD dst_unused:UNUSED_PAD src0_sel:DWORD src1_sel:WORD_1
	v_pk_mul_f32 v[4:5], v[4:5], v[12:13]
	v_and_b32_sdwa v0, v7, v236 dst_sel:DWORD dst_unused:UNUSED_PAD src0_sel:WORD_1 src1_sel:DWORD
	v_and_b32_sdwa v8, v6, v236 dst_sel:DWORD dst_unused:UNUSED_PAD src0_sel:WORD_1 src1_sel:DWORD
	v_add3_u32 v6, v6, v8, s80
	v_add3_u32 v0, v7, v0, s80
	v_and_b32_sdwa v7, v5, v236 dst_sel:DWORD dst_unused:UNUSED_PAD src0_sel:WORD_1 src1_sel:DWORD
	v_and_b32_sdwa v8, v4, v236 dst_sel:DWORD dst_unused:UNUSED_PAD src0_sel:WORD_1 src1_sel:DWORD
	v_add3_u32 v5, v5, v7, s80
	v_add3_u32 v4, v4, v8, s80
	v_and_b32_e32 v5, 0xffff0000, v5
	v_and_b32_e32 v4, 0xffff0000, v4
	v_or_b32_sdwa v5, v5, v0 dst_sel:DWORD dst_unused:UNUSED_PAD src0_sel:DWORD src1_sel:WORD_1
	v_or_b32_sdwa v4, v4, v6 dst_sel:DWORD dst_unused:UNUSED_PAD src0_sel:DWORD src1_sel:WORD_1
	global_store_dwordx4 v[48:49], v[30:33], off
	global_store_dwordx4 v[46:47], v[34:37], off
	global_store_dwordx4 v[44:45], v[2:5], off
	global_store_dwordx4 v[42:43], v[26:29], off
	s_andn2_b64 exec, exec, s[42:43]
	s_cbranch_execz .LBB0_820
.LBB0_784:
	v_ashrrev_i32_e32 v42, 4, v131
	v_and_b32_e32 v43, -4, v42
	v_cmp_lt_i32_e32 vcc, s80, v43
	s_and_saveexec_b64 s[0:1], vcc
	s_xor_b64 s[4:5], exec, s[0:1]
	v_and_b32_e32 v45, 0xfc, v42
	s_or_saveexec_b64 s[4:5], s[4:5]
	v_mov_b32_e32 v46, 0x100
	s_xor_b64 exec, exec, s[4:5]
	v_ashrrev_i32_e32 v0, 31, v43
	v_lshrrev_b32_e32 v0, 20, v0
	v_add_u32_e32 v0, v43, v0
	v_and_b32_e32 v0, 0xfffff000, v0
	v_sub_u32_e32 v45, v43, v0
	v_mov_b32_e32 v46, 0x1000
	s_or_b64 exec, exec, s[4:5]
	v_readlane_b32 s0, v252, 26
	v_readlane_b32 s1, v252, 27
	v_and_b32_e32 v34, 0x1f8, v130
	v_lshlrev_b32_e32 v0, 1, v34
	v_mov_b64_e32 v[2:3], s[0:1]
	v_mad_i64_i32 v[2:3], s[0:1], v43, s88, v[2:3]
	v_lshl_add_u64 v[38:39], v[2:3], 0, v[0:1]
	v_mov_b32_e32 v35, 0
	v_cmp_lt_i32_e64 s[4:5], 0, v45
	v_mov_b32_e32 v36, 0
	s_and_saveexec_b64 s[44:45], s[4:5]
	s_cbranch_execz .LBB0_790
	v_add_co_u32_e32 v2, vcc, 0xffffd000, v38
	s_nop 1
	v_addc_co_u32_e32 v3, vcc, -1, v39, vcc
	global_load_dword v36, v[2:3], off offset:-512

.LBB0_804:
	s_or_b64 exec, exec, s[44:45]
	v_add_co_u32_e32 v2, vcc, 0x3000, v38
	global_load_dwordx4 v[26:29], v[38:39], off offset:1024
	global_load_dwordx4 v[30:33], v[38:39], off offset:2048
	v_addc_co_u32_e32 v3, vcc, 0, v39, vcc
	global_load_dwordx4 v[22:25], v[2:3], off offset:2560
	global_load_dwordx4 v[18:21], v[2:3], off offset:3584
	v_add_co_u32_e32 v2, vcc, 0x7000, v38
	v_add_u32_e32 v45, 4, v45
	s_nop 0
	v_addc_co_u32_e32 v3, vcc, 0, v39, vcc
	v_add_co_u32_e32 v6, vcc, 0xa000, v38
	global_load_dwordx4 v[10:13], v[2:3], off
	global_load_dwordx4 v[14:17], v[2:3], off offset:1024
	v_addc_co_u32_e32 v7, vcc, 0, v39, vcc
	global_load_dwordx4 v[2:5], v[6:7], off offset:1536
	s_nop 0
	global_load_dwordx4 v[6:9], v[6:7], off offset:2560
	s_mov_b64 s[100:101], 0xa000
	v_lshl_add_u64 v[206:207], v[38:39], 0, s[100:101]
	global_load_dwordx4 v[170:173], v[206:207], off offset:512
	v_lshlrev_b32_e32 v217, 2, v34
	global_load_dwordx4 v[174:177], v217, s[36:37] offset:16
	global_load_dwordx4 v[178:181], v217, s[36:37]
	global_load_dwordx4 v[182:185], v217, s[36:37] offset:2064
	global_load_dwordx4 v[186:189], v217, s[36:37] offset:2048
	v_add_u32_e32 v218, 0x1000, v217
	global_load_dwordx4 v[190:193], v218, s[36:37]
	global_load_dwordx4 v[194:197], v218, s[36:37] offset:16
	global_load_dwordx4 v[198:201], v[38:39], off
	s_mov_b64 s[100:101], 0x3000
	v_lshl_add_u64 v[206:207], v[38:39], 0, s[100:101]
	global_load_dwordx4 v[202:205], v[206:207], off offset:1536
	s_mov_b64 s[100:101], 0x6000
	v_lshl_add_u64 v[206:207], v[38:39], 0, s[100:101]
	global_load_dwordx4 v[222:225], v[206:207], off offset:3072
	v_cmp_lt_i32_e64 s[4:5], v45, v46
	v_mov_b32_e32 v46, 0
	v_mov_b32_e32 v45, 0
	s_and_saveexec_b64 s[44:45], s[4:5]
	s_cbranch_execz .LBB0_806
	v_add_co_u32_e32 v50, vcc, 0xd000, v38
	s_nop 1
	v_addc_co_u32_e32 v51, vcc, 0, v39, vcc
	global_load_dword v45, v[50:51], off offset:3072
